# baseline (speedup 1.0000x reference)
.LBB1_21:
	s_or_b64 exec, exec, s[4:5]
	s_lshr_b32 s4, s18, 16
	v_cvt_f32_u32_e32 v3, s4
	v_lshlrev_b64 v[8:9], 11, v[6:7]
	v_lshl_add_u64 v[8:9], s[16:17], 0, v[8:9]
	s_and_b32 s10, s18, 0xffff
	v_div_scale_f32 v4, s[4:5], v3, v3, 1.0
	v_rcp_f32_e32 v12, v4
	v_div_scale_f32 v13, vcc, 1.0, v3, 1.0
	v_readlane_b32 s44, v16, 0
	v_fma_f32 v17, -v4, v12, 1.0
	v_readlane_b32 s45, v16, 1
	v_fmac_f32_e32 v12, v17, v12
	v_readlane_b32 s46, v16, 2
	v_mul_f32_e32 v17, v13, v12
	v_readlane_b32 s47, v16, 3
	v_fma_f32 v18, -v4, v17, v13
	v_readlane_b32 s48, v16, 4
	v_fmac_f32_e32 v17, v18, v12
	v_readlane_b32 s49, v16, 5
	v_fma_f32 v4, -v4, v17, v13
	v_readlane_b32 s50, v16, 6
	v_readlane_b32 s51, v16, 7
	v_div_fmas_f32 v4, v4, v12, v17
	v_readlane_b32 s52, v16, 8
	v_readlane_b32 s53, v16, 9
	v_div_fixup_f32 v4, v4, v3, 1.0
	v_readlane_b32 s54, v16, 10
	v_readlane_b32 s55, v16, 11
	v_mov_b32_e32 v3, 0
	v_readlane_b32 s56, v16, 12
	v_readlane_b32 s57, v16, 13
	v_lshl_add_u64 v[8:9], v[2:3], 2, v[8:9]
	v_readlane_b32 s58, v16, 14
	v_readlane_b32 s59, v16, 15
	v_cndmask_b32_e64 v12, 0, v4, s[44:45]
	global_store_dword v[8:9], v12, off
	v_cndmask_b32_e64 v12, 0, v4, s[46:47]
	global_store_dword v[8:9], v12, off offset:256
	v_cndmask_b32_e64 v12, 0, v4, s[48:49]
	global_store_dword v[8:9], v12, off offset:512
	v_cndmask_b32_e64 v12, 0, v4, s[50:51]
	global_store_dword v[8:9], v12, off offset:768
	v_cndmask_b32_e64 v12, 0, v4, s[52:53]
	global_store_dword v[8:9], v12, off offset:1024
	v_cndmask_b32_e64 v12, 0, v4, s[54:55]
	global_store_dword v[8:9], v12, off offset:1280
	v_cndmask_b32_e64 v12, 0, v4, s[56:57]
	global_store_dword v[8:9], v12, off offset:1536
	v_cndmask_b32_e64 v12, 0, v4, s[58:59]
	global_store_dword v[8:9], v12, off offset:1792
	v_cmp_le_u32_e64 s[4:5], s10, v2
	v_cmp_gt_u32_e32 vcc, 24, v2
	s_and_b64 s[14:15], vcc, s[4:5]
	s_and_saveexec_b64 s[4:5], s[14:15]
	s_cbranch_execz .LBB1_23
	v_mad_u64_u32 v[8:9], s[8:9], v6, 48, s[8:9]
	v_mad_u32_u24 v9, v7, 48, v9
	v_add_u32_e32 v12, -10, v2
	v_cmp_gt_u32_e32 vcc, 4, v12
	s_nop 1
	v_cndmask_b32_e64 v12, 0, 6, vcc
	v_xor_b32_e32 v12, v2, v12
	v_mov_b32_e32 v13, 0
	v_lshl_add_u64 v[8:9], v[12:13], 1, v[8:9]
	v_mov_b32_e32 v3, 0x2000
	global_store_short v[8:9], v3, off

	.amdhsa_kernel _Z7k2_elimPKjPKiPiS2_PfP15HIP_vector_typeIiLj4EEPKfS4_PtSA_
		.amdhsa_group_segment_fixed_size 34880
		.amdhsa_private_segment_fixed_size 0
		.amdhsa_kernarg_size 80
		.amdhsa_user_sgpr_count 2
		.amdhsa_user_sgpr_dispatch_ptr 0
		.amdhsa_user_sgpr_queue_ptr 0
		.amdhsa_user_sgpr_kernarg_segment_ptr 1
		.amdhsa_user_sgpr_dispatch_id 0
		.amdhsa_user_sgpr_kernarg_preload_length 0
		.amdhsa_user_sgpr_kernarg_preload_offset 0
		.amdhsa_user_sgpr_private_segment_size 0
		.amdhsa_uses_dynamic_stack 0
		.amdhsa_enable_private_segment 0
		.amdhsa_system_sgpr_workgroup_id_x 1
		.amdhsa_system_sgpr_workgroup_id_y 0
		.amdhsa_system_sgpr_workgroup_id_z 0
		.amdhsa_system_sgpr_workgroup_info 0
		.amdhsa_system_vgpr_workitem_id 0
		.amdhsa_next_free_vgpr 35
		.amdhsa_next_free_sgpr 60
		.amdhsa_accum_offset 36
		.amdhsa_reserve_vcc 1
		.amdhsa_float_round_mode_32 0
		.amdhsa_float_round_mode_16_64 0
		.amdhsa_float_denorm_mode_32 3
		.amdhsa_float_denorm_mode_16_64 3
		.amdhsa_dx10_clamp 1
		.amdhsa_ieee_mode 1
		.amdhsa_fp16_overflow 0
		.amdhsa_tg_split 0
		.amdhsa_exception_fp_ieee_invalid_op 0
		.amdhsa_exception_fp_denorm_src 0
		.amdhsa_exception_fp_ieee_div_zero 0
		.amdhsa_exception_fp_ieee_overflow 0
		.amdhsa_exception_fp_ieee_underflow 0
		.amdhsa_exception_fp_ieee_inexact 0
		.amdhsa_exception_int_div_zero 0
	.end_amdhsa_kernel

amdhsa.kernels:
  - .agpr_count:     0
    .args:
      - .actual_access:  read_only
        .address_space:  global
        .offset:         0
        .size:           8
        .value_kind:     global_buffer
      - .actual_access:  read_only
        .address_space:  global
        .offset:         8
        .size:           8
        .value_kind:     global_buffer
      - .actual_access:  write_only
        .address_space:  global
        .offset:         16
        .size:           8
        .value_kind:     global_buffer
      - .actual_access:  write_only
        .address_space:  global
        .offset:         24
        .size:           8
        .value_kind:     global_buffer
      - .actual_access:  write_only
        .address_space:  global
        .offset:         32
        .size:           8
        .value_kind:     global_buffer
    .group_segment_fixed_size: 1024
    .kernarg_segment_align: 8
    .kernarg_segment_size: 40
    .language:       OpenCL C
    .language_version:
      - 2
      - 0
    .max_flat_workgroup_size: 256
    .name:           _Z7k1_packPKfS0_PmPiP15HIP_vector_typeIfLj4EE
    .private_segment_fixed_size: 0
    .sgpr_count:     16
    .sgpr_spill_count: 0
    .symbol:         _Z7k1_packPKfS0_PmPiP15HIP_vector_typeIfLj4EE.kd
    .uniform_work_group_size: 1
    .uses_dynamic_stack: false
    .vgpr_count:     33
    .vgpr_spill_count: 0
    .wavefront_size: 64
  - .agpr_count:     0
    .args:
      - .actual_access:  read_only
        .address_space:  global
        .offset:         0
        .size:           8
        .value_kind:     global_buffer
      - .actual_access:  read_only
        .address_space:  global
        .offset:         8
        .size:           8
        .value_kind:     global_buffer
      - .actual_access:  write_only
        .address_space:  global
        .offset:         16
        .size:           8
        .value_kind:     global_buffer
      - .actual_access:  read_only
        .address_space:  global
        .offset:         24
        .size:           8
        .value_kind:     global_buffer
      - .actual_access:  write_only
        .address_space:  global
        .offset:         32
        .size:           8
        .value_kind:     global_buffer
      - .actual_access:  write_only
        .address_space:  global
        .offset:         40
        .size:           8
        .value_kind:     global_buffer
      - .actual_access:  read_only
        .address_space:  global
        .offset:         48
        .size:           8
        .value_kind:     global_buffer
      - .address_space:  global
        .offset:         56
        .size:           8
        .value_kind:     global_buffer
      - .actual_access:  write_only
        .address_space:  global
        .offset:         64
        .size:           8
        .value_kind:     global_buffer
      - .actual_access:  write_only
        .address_space:  global
        .offset:         72
        .size:           8
        .value_kind:     global_buffer
    .group_segment_fixed_size: 34880
    .kernarg_segment_align: 8
    .kernarg_segment_size: 80
    .language:       OpenCL C
    .language_version:
      - 2
      - 0
    .max_flat_workgroup_size: 512
    .name:           _Z7k2_elimPKjPKiPiS2_PfP15HIP_vector_typeIiLj4EEPKfS4_PtSA_
    .private_segment_fixed_size: 0
    .sgpr_count:     66
    .sgpr_spill_count: 0
    .symbol:         _Z7k2_elimPKjPKiPiS2_PfP15HIP_vector_typeIiLj4EEPKfS4_PtSA_.kd
    .uniform_work_group_size: 1
    .uses_dynamic_stack: false
    .vgpr_count:     35
    .vgpr_spill_count: 0
    .wavefront_size: 64
  - .agpr_count:     0
    .args:
      - .actual_access:  read_only
        .address_space:  global
        .offset:         0
        .size:           8
        .value_kind:     global_buffer
      - .actual_access:  read_only
        .address_space:  global
        .offset:         8
        .size:           8
        .value_kind:     global_buffer
      - .actual_access:  read_only
        .address_space:  global
        .offset:         16
        .size:           8
        .value_kind:     global_buffer
      - .actual_access:  read_only
        .address_space:  global
        .offset:         24
        .size:           8
        .value_kind:     global_buffer
      - .actual_access:  read_only
        .address_space:  global
        .offset:         32
        .size:           8
        .value_kind:     global_buffer
      - .actual_access:  read_only
        .address_space:  global
        .offset:         40
        .size:           8
        .value_kind:     global_buffer
      - .actual_access:  write_only
        .address_space:  global
        .offset:         48
        .size:           8
        .value_kind:     global_buffer
    .group_segment_fixed_size: 80064
    .kernarg_segment_align: 8
    .kernarg_segment_size: 56
    .language:       OpenCL C
    .language_version:
      - 2
      - 0
    .max_flat_workgroup_size: 256
    .name:           _Z8k3_chainPKfPK15HIP_vector_typeIiLj4EEPKtS6_S0_S0_Pf
    .private_segment_fixed_size: 0
    .sgpr_count:     28
    .sgpr_spill_count: 0
    .symbol:         _Z8k3_chainPKfPK15HIP_vector_typeIiLj4EEPKtS6_S0_S0_Pf.kd
    .uniform_work_group_size: 1
    .uses_dynamic_stack: false
    .vgpr_count:     184
    .vgpr_spill_count: 0
    .wavefront_size: 64
